# P5: second token's loads issued with the first token's (own registers), waits re-derived
# baseline (speedup 1.0000x reference)
; __device__ __forceinline__ void phase4_post(const Args& a, LAS unsigned char* lds, int lane, int wave, int vcu, int G) {
;     ...
;     for (int t0 = vcu * 8 + wave; t0 < NT; t0 += 2 * G * 8, ++it) {
;         ci = conv_decode(a, 2 * I_E + N_DOWN_CHAIN + N_DOWN_PREP + it * (G * 8) + vcu * 8 + wave); conv_load(ct, ci, lane);
; #pragma unroll
;         for (int h2 = 0; h2 < 2; ++h2) { const int t = t0 + h2 * G * 8; if (t < NT) {
;         const size_t o = (size_t)t * 1024 + 16 * lane;
;         const v4u f0 = __builtin_nontemporal_load((const v4u*)(OF + o)), f1 = __builtin_nontemporal_load((const v4u*)(OF + o + 8)), b0 = __builtin_nontemporal_load((const v4u*)(OB + o)), b1 = __builtin_nontemporal_load((const v4u*)(OB + o + 8)), r0 = __builtin_nontemporal_load((const v4u*)(Rr + o)), r1 = __builtin_nontemporal_load((const v4u*)(Rr + o + 8));
;         float x[16], r[16];
; #pragma unroll
;         for (int w = 0; w < 4; ++w) { x[2 * w] = bflo(f0[w]) + bflo(b0[w]); x[2 * w + 1] = bfhi(f0[w]) + bfhi(b0[w]); x[8 + 2 * w] = bflo(f1[w]) + bflo(b1[w]); x[8 + 2 * w + 1] = bfhi(f1[w]) + bfhi(b1[w]);
;             r[2 * w] = bflo(r0[w]); r[2 * w + 1] = bfhi(r0[w]); r[8 + 2 * w] = bflo(r1[w]); r[8 + 2 * w + 1] = bfhi(r1[w]); }
;         float ss = 0.f;
; #pragma unroll
;         for (int q = 0; q < 16; ++q) ss += x[q] * x[q];
;         ss += dppf<0xB1>(ss); ss += dppf<0x4E>(ss); ss += dppf<0x141>(ss); ss += dppf<0x140>(ss);
;         const float sc = rsqrtf(ss * (1.f / 256.f) + EPS);
.LBB0_934:
	s_ashr_i32 s15, s14, 31
	s_lshl_b64 s[16:17], s[14:15], 11
	v_lshl_or_b32 v18, v52, 1, s16
	v_mov_b32_e32 v19, s17
	v_lshl_add_u64 v[20:21], s[0:1], 0, v[18:19]
	v_lshl_add_u64 v[22:23], s[6:7], 0, v[18:19]
	global_load_dwordx4 v[74:77], v[20:21], off nt
	global_load_dwordx4 v[80:83], v[22:23], off nt
	global_load_dwordx4 v[84:87], v[20:21], off offset:16 nt
	global_load_dwordx4 v[88:91], v[22:23], off offset:16 nt
	v_lshl_add_u64 v[18:19], s[4:5], 0, v[18:19]
	global_load_dwordx4 v[100:103], v[18:19], off nt
	global_load_dwordx4 v[104:107], v[18:19], off offset:16 nt
	s_lshl_b32 s36, s26, 11
	s_mov_b32 s37, 0
	v_lshl_add_u64 v[152:153], v[20:21], 0, s[36:37]
	v_lshl_add_u64 v[154:155], v[22:23], 0, s[36:37]
	v_lshl_add_u64 v[156:157], v[18:19], 0, s[36:37]
	global_load_dwordx4 v[128:131], v[152:153], off nt
	global_load_dwordx4 v[132:135], v[154:155], off nt
	global_load_dwordx4 v[136:139], v[152:153], off offset:16 nt
	global_load_dwordx4 v[140:143], v[154:155], off offset:16 nt
	global_load_dwordx4 v[144:147], v[156:157], off nt
	global_load_dwordx4 v[148:151], v[156:157], off offset:16 nt
	s_lshl_b32 s12, s3, 6
	v_or_b32_e32 v2, s12, v1
	v_or_b32_e32 v4, s12, v95
	v_or_b32_e32 v6, s12, v96
	v_or_b32_e32 v8, s12, v97
	v_mul_hi_i32_i24_e32 v19, s20, v2
	v_mul_i32_i24_e32 v18, s20, v2
	v_mul_hi_i32_i24_e32 v21, s20, v4
	v_mul_i32_i24_e32 v20, s20, v4
	v_mul_hi_i32_i24_e32 v23, s20, v6
	v_mul_i32_i24_e32 v22, s20, v6
	v_mul_hi_i32_i24_e32 v25, s20, v8
	v_mul_i32_i24_e32 v24, s20, v8
	v_or_b32_e32 v4, 32, v2
	v_or_b32_e32 v6, 40, v2
	v_or_b32_e32 v8, 48, v2
	v_or_b32_e32 v2, 56, v2
	v_mul_hi_i32_i24_e32 v27, s20, v4
	v_mul_i32_i24_e32 v26, s20, v4
	v_mul_hi_i32_i24_e32 v29, s20, v6
	v_mul_i32_i24_e32 v28, s20, v6
	v_mul_hi_i32_i24_e32 v31, s20, v8
	v_mul_i32_i24_e32 v30, s20, v8
	v_mul_hi_i32_i24_e32 v33, s20, v2
	v_mul_i32_i24_e32 v32, s20, v2
	s_ashr_i32 s3, s2, 31
	s_lshl_b64 s[2:3], s[2:3], 2
	v_lshl_add_u64 v[18:19], v[18:19], 2, s[18:19]
	v_lshl_add_u64 v[20:21], v[20:21], 2, s[18:19]
	v_lshl_add_u64 v[22:23], v[22:23], 2, s[18:19]
	v_lshl_add_u64 v[24:25], v[24:25], 2, s[18:19]
	v_lshl_add_u64 v[18:19], v[18:19], 0, s[2:3]
	v_lshl_add_u64 v[20:21], v[20:21], 0, s[2:3]
	v_lshl_add_u64 v[22:23], v[22:23], 0, s[2:3]
	v_lshl_add_u64 v[26:27], v[26:27], 2, s[18:19]
	v_lshl_add_u64 v[28:29], v[28:29], 2, s[18:19]
	v_lshl_add_u64 v[30:31], v[30:31], 2, s[18:19]
	v_lshl_add_u64 v[32:33], v[32:33], 2, s[18:19]
	v_lshl_add_u64 v[24:25], v[24:25], 0, s[2:3]
	v_lshl_add_u64 v[18:19], v[18:19], 0, v[50:51]
	v_lshl_add_u64 v[20:21], v[20:21], 0, v[50:51]
	v_lshl_add_u64 v[22:23], v[22:23], 0, v[50:51]
	v_lshl_add_u64 v[26:27], v[26:27], 0, s[2:3]
	v_lshl_add_u64 v[28:29], v[28:29], 0, s[2:3]
	v_lshl_add_u64 v[34:35], v[30:31], 0, s[2:3]
	v_lshl_add_u64 v[36:37], v[32:33], 0, s[2:3]
	v_lshl_add_u64 v[24:25], v[24:25], 0, v[50:51]
	global_load_dwordx4 v[46:49], v[18:19], off nt
	global_load_dwordx4 v[42:45], v[20:21], off nt
	global_load_dwordx4 v[38:41], v[22:23], off nt
	global_load_dwordx4 v[30:33], v[24:25], off nt
	v_lshl_add_u64 v[18:19], v[26:27], 0, v[50:51]
	v_lshl_add_u64 v[20:21], v[28:29], 0, v[50:51]
	v_lshl_add_u64 v[22:23], v[34:35], 0, v[50:51]
	v_lshl_add_u64 v[78:79], v[36:37], 0, v[50:51]
	global_load_dwordx4 v[34:37], v[18:19], off nt
	global_load_dwordx4 v[26:29], v[20:21], off nt
	s_nop 0
	global_load_dwordx4 v[22:25], v[22:23], off nt
	s_nop 0
	global_load_dwordx4 v[18:21], v[78:79], off nt
	s_add_i32 s14, s14, s26
	s_cmpk_gt_i32 s14, 0x3fff
	s_waitcnt vmcnt(18)
	v_lshlrev_b32_e32 v4, 16, v80
	v_lshlrev_b32_e32 v2, 16, v74
	v_and_b32_e32 v6, 0xffff0000, v80
	v_and_b32_e32 v8, 0xffff0000, v74
	s_waitcnt vmcnt(17)
	v_lshlrev_b32_e32 v10, 16, v84
	s_waitcnt vmcnt(16)
	v_lshlrev_b32_e32 v12, 16, v88
	v_and_b32_e32 v14, 0xffff0000, v88
	v_and_b32_e32 v16, 0xffff0000, v84
	v_add_f32_e32 v2, v4, v2
	v_add_f32_e32 v4, v6, v8
	v_add_f32_e32 v6, v12, v10
	v_lshlrev_b32_e32 v10, 16, v75
	v_lshlrev_b32_e32 v12, 16, v81
	v_add_f32_e32 v8, v14, v16
	v_add_f32_e32 v10, v12, v10
	v_and_b32_e32 v12, 0xffff0000, v81
	v_and_b32_e32 v14, 0xffff0000, v75
	v_add_f32_e32 v12, v12, v14
	v_lshlrev_b32_e32 v14, 16, v76
	v_lshlrev_b32_e32 v16, 16, v82
	v_add_f32_e32 v58, v16, v14
	v_and_b32_e32 v14, 0xffff0000, v82
	v_and_b32_e32 v16, 0xffff0000, v76
	v_add_f32_e32 v60, v14, v16
	v_lshlrev_b32_e32 v14, 16, v77
	v_lshlrev_b32_e32 v16, 16, v83
	v_add_f32_e32 v62, v16, v14
	v_and_b32_e32 v14, 0xffff0000, v83
	v_and_b32_e32 v16, 0xffff0000, v77
	v_add_f32_e32 v64, v14, v16
	v_mul_f32_e32 v14, v2, v2
	v_fmac_f32_e32 v14, v4, v4
	v_fmac_f32_e32 v14, v10, v10
	v_fmac_f32_e32 v14, v12, v12
	v_fmac_f32_e32 v14, v58, v58
	v_fmac_f32_e32 v14, v60, v60
	v_fmac_f32_e32 v14, v62, v62
	v_lshlrev_b32_e32 v79, 16, v89
	v_lshlrev_b32_e32 v109, 16, v85
	v_and_b32_e32 v78, 0xffff0000, v89
	v_and_b32_e32 v108, 0xffff0000, v85
	v_fmac_f32_e32 v14, v64, v64
	v_pk_add_f32 v[108:109], v[108:109], v[78:79]
	v_fmac_f32_e32 v14, v6, v6
	v_lshlrev_b32_e32 v115, 16, v90
	v_lshlrev_b32_e32 v117, 16, v86
	v_and_b32_e32 v114, 0xffff0000, v90
	v_and_b32_e32 v116, 0xffff0000, v86
	v_pk_mul_f32 v[122:123], v[108:109], v[108:109]
	v_fmac_f32_e32 v14, v8, v8
	v_pk_add_f32 v[114:115], v[116:117], v[114:115]
	v_add_f32_e32 v14, v123, v14
	v_lshlrev_b32_e32 v119, 16, v91
	v_lshlrev_b32_e32 v121, 16, v87
	v_and_b32_e32 v118, 0xffff0000, v91
	v_and_b32_e32 v120, 0xffff0000, v87
	v_pk_mul_f32 v[116:117], v[114:115], v[114:115]
	v_add_f32_e32 v14, v122, v14
	v_pk_add_f32 v[78:79], v[120:121], v[118:119]
	v_add_f32_e32 v14, v117, v14
	v_pk_mul_f32 v[118:119], v[78:79], v[78:79]
	v_add_f32_e32 v14, v116, v14
	v_add_f32_e32 v14, v119, v14
	v_add_f32_e32 v14, v118, v14
	s_waitcnt vmcnt(15)
; __device__ __forceinline__ float silu_f(float x) { return x * __builtin_amdgcn_rcpf(1.f + __expf(-x)); }
; __device__ __forceinline__ void phase4_post(const Args& a, LAS unsigned char* lds, int lane, int wave, int vcu, int G) {
;     ...
;         const float sc = rsqrtf(ss * (1.f / 256.f) + EPS);
;         float y[16];
; #pragma unroll
;         for (int q = 0; q < 16; ++q) y[q] = x[q] * sc * g4[q >> 2][q & 3] * silu_f(r[q]);
;         v4u o0;
; #pragma unroll
;         for (int w = 0; w < 4; ++w) o0[w] = pk4_fp8(y[4 * w] * SC_Y, y[4 * w + 1] * SC_Y, y[4 * w + 2] * SC_Y, y[4 * w + 3] * SC_Y);
;         *(v4u*)(Y + (size_t)t * 2048 + 16 * lane) = o0;
;         } }
	v_and_b32_e32 v88, 0xffff0000, v100
	v_lshlrev_b32_e32 v84, 16, v100
	v_add_f32_dpp v14, v14, v14 quad_perm:[1,0,3,2] row_mask:0xf bank_mask:0xf bound_ctrl:1
	s_waitcnt vmcnt(14)
	v_lshlrev_b32_e32 v92, 16, v104
	v_and_b32_e32 v100, 0xffff0000, v104
	v_add_f32_dpp v14, v14, v14 quad_perm:[2,3,0,1] row_mask:0xf bank_mask:0xf bound_ctrl:1
	v_lshlrev_b32_e32 v104, 16, v101
	v_and_b32_e32 v110, 0xffff0000, v101
	v_add_f32_dpp v14, v14, v14 row_half_mirror row_mask:0xf bank_mask:0xf bound_ctrl:1
	v_mul_f32_e32 v66, 0xbfb8aa3b, v84
	v_exp_f32_e32 v66, v66
	v_add_f32_dpp v14, v14, v14 row_mirror row_mask:0xf bank_mask:0xf bound_ctrl:1
	v_fmamk_f32 v14, v14, 0x3b800000, v94
	v_mul_f32_e32 v16, 0x4b800000, v14
	v_cmp_gt_f32_e32 vcc, s24, v14
	v_lshlrev_b32_e32 v82, 16, v102
	v_and_b32_e32 v86, 0xffff0000, v102
	v_cndmask_b32_e32 v14, v14, v16, vcc
	v_rsq_f32_e32 v14, v14
	v_lshlrev_b32_e32 v90, 16, v103
	v_lshlrev_b32_e32 v112, 16, v105
	v_and_b32_e32 v80, 0xffff0000, v105
	v_mul_f32_e32 v16, 0x45800000, v14
	v_cndmask_b32_e32 v117, v14, v16, vcc
	v_mul_f32_e32 v14, 0xbfb8aa3b, v88
	v_exp_f32_e32 v14, v14
	v_mul_f32_e32 v85, v2, v117
	v_mul_f32_e32 v89, v4, v117
	v_mul_f32_e32 v4, 0xbfb8aa3b, v110
	v_add_f32_e32 v2, 1.0, v14
	v_rcp_f32_e32 v14, v2
	v_mul_f32_e32 v2, 0xbfb8aa3b, v104
	v_exp_f32_e32 v2, v2
	v_exp_f32_e32 v4, v4
	v_add_f32_e32 v16, 1.0, v66
	v_rcp_f32_e32 v72, v16
	v_add_f32_e32 v2, 1.0, v2
	v_rcp_f32_e32 v70, v2
	v_add_f32_e32 v2, 1.0, v4
	v_rcp_f32_e32 v16, v2
	v_mul_f32_e32 v2, 0xbfb8aa3b, v82
	v_exp_f32_e32 v2, v2
	v_mul_f32_e32 v4, 0xbfb8aa3b, v86
	v_exp_f32_e32 v4, v4
	v_and_b32_e32 v102, 0xffff0000, v103
	v_add_f32_e32 v2, 1.0, v2
	v_rcp_f32_e32 v68, v2
	v_add_f32_e32 v2, 1.0, v4
	v_mul_f32_e32 v105, v10, v117
	v_rcp_f32_e32 v10, v2
	v_mul_f32_e32 v2, 0xbfb8aa3b, v90
	v_exp_f32_e32 v2, v2
	v_mul_f32_e32 v4, 0xbfb8aa3b, v102
	v_exp_f32_e32 v4, v4
	v_mul_f32_e32 v111, v12, v117
	v_add_f32_e32 v2, 1.0, v2
	v_rcp_f32_e32 v66, v2
	v_add_f32_e32 v2, 1.0, v4
	v_rcp_f32_e32 v12, v2
	v_mul_f32_e32 v2, 0xbfb8aa3b, v92
	v_exp_f32_e32 v2, v2
	v_mul_f32_e32 v4, 0xbfb8aa3b, v100
	v_exp_f32_e32 v4, v4
	v_mul_f32_e32 v103, v64, v117
	v_add_f32_e32 v2, 1.0, v2
	v_rcp_f32_e32 v64, v2
	v_add_f32_e32 v2, 1.0, v4
	v_mul_f32_e32 v93, v6, v117
	v_rcp_f32_e32 v6, v2
	v_mul_f32_e32 v2, 0xbfb8aa3b, v112
	v_exp_f32_e32 v2, v2
	v_mul_f32_e32 v4, 0xbfb8aa3b, v80
	v_exp_f32_e32 v4, v4
	v_lshlrev_b32_e32 v76, 16, v106
	v_add_f32_e32 v2, 1.0, v2
	v_mul_f32_e32 v91, v62, v117
	v_rcp_f32_e32 v62, v2
	v_add_f32_e32 v2, 1.0, v4
	v_and_b32_e32 v74, 0xffff0000, v106
	v_mul_f32_e32 v101, v8, v117
	v_rcp_f32_e32 v8, v2
	v_mul_f32_e32 v2, 0xbfb8aa3b, v76
	v_exp_f32_e32 v2, v2
	v_mul_f32_e32 v4, 0xbfb8aa3b, v74
	v_exp_f32_e32 v4, v4
	v_mul_f32_e32 v87, v60, v117
	v_add_f32_e32 v2, 1.0, v2
	v_rcp_f32_e32 v60, v2
	v_add_f32_e32 v2, 1.0, v4
	v_rcp_f32_e32 v2, v2
	v_lshlrev_b32_e32 v106, 16, v107
	v_mul_f32_e32 v75, v114, v117
	v_and_b32_e32 v116, 0xffff0000, v107
	v_pk_mul_f32 v[74:75], v[2:3], v[74:75]
	v_mul_f32_e32 v2, 0xbfb8aa3b, v106
	v_exp_f32_e32 v2, v2
	v_mul_f32_e32 v4, 0xbfb8aa3b, v116
	v_exp_f32_e32 v4, v4
	v_mul_f32_e32 v83, v58, v117
	v_add_f32_e32 v2, 1.0, v2
	v_rcp_f32_e32 v58, v2
	v_add_f32_e32 v2, 1.0, v4
	v_rcp_f32_e32 v4, v2
	v_pk_mul_f32 v[84:85], v[72:73], v[84:85]
	v_mul_f32_e32 v77, v115, v117
	v_mul_f32_e32 v72, v84, v85
	v_pk_mul_f32 v[84:85], v[14:15], v[88:89]
	v_pk_mul_f32 v[76:77], v[60:61], v[76:77]
	v_mul_f32_e32 v107, v79, v117
	v_mul_f32_e32 v14, v84, v85
	v_mul_f32_e32 v113, v109, v117
	v_mul_f32_e32 v81, v108, v117
	v_mul_f32_e32 v60, v76, v77
	v_mul_f32_e32 v77, v74, v75
	v_pk_mul_f32 v[74:75], v[58:59], v[106:107]
	v_mul_f32_e32 v117, v78, v117
	v_mul_f32_e32 v2, v74, v75
	v_pk_mul_f32 v[74:75], v[4:5], v[116:117]
	v_mul_f32_e32 v58, 0x41000000, v72
	v_mul_f32_e32 v14, 0x41000000, v14
	v_pk_mul_f32 v[84:85], v[70:71], v[104:105]
	v_mul_f32_e32 v4, v74, v75
	v_med3_f32 v58, v58, s25, v99
	v_med3_f32 v14, v14, s25, v99
	v_mov_b32_e32 v74, v51
	v_mul_f32_e32 v70, v84, v85
	v_pk_mul_f32 v[84:85], v[16:17], v[110:111]
	v_cvt_pk_fp8_f32 v74, v58, v14
	v_mul_f32_e32 v16, v84, v85
	v_pk_mul_f32 v[82:83], v[68:69], v[82:83]
	v_mul_f32_e32 v70, 0x41000000, v70
	v_mul_f32_e32 v68, v82, v83
	v_pk_mul_f32 v[82:83], v[10:11], v[86:87]
	v_mul_f32_e32 v14, 0x41000000, v16
	v_mul_f32_e32 v10, v82, v83
	v_med3_f32 v16, v70, s25, v99
	v_med3_f32 v14, v14, s25, v99
	v_cvt_pk_fp8_f32 v74, v16, v14 op_sel:[0,0,1]
	v_mul_f32_e32 v14, 0x41000000, v68
	v_mul_f32_e32 v10, 0x41000000, v10
	v_pk_mul_f32 v[82:83], v[66:67], v[90:91]
	v_med3_f32 v14, v14, s25, v99
	v_med3_f32 v10, v10, s25, v99
	v_mov_b32_e32 v75, v51
	v_mul_f32_e32 v66, v82, v83
	v_pk_mul_f32 v[82:83], v[12:13], v[102:103]
	v_cvt_pk_fp8_f32 v75, v14, v10
	v_mul_f32_e32 v12, v82, v83
	v_pk_mul_f32 v[82:83], v[64:65], v[92:93]
	v_mul_f32_e32 v16, 0x41000000, v66
	v_mul_f32_e32 v64, v82, v83
	v_pk_mul_f32 v[82:83], v[6:7], v[100:101]
	v_mul_f32_e32 v10, 0x41000000, v12
	v_mul_f32_e32 v6, v82, v83
	v_med3_f32 v12, v16, s25, v99
	v_med3_f32 v10, v10, s25, v99
	v_cvt_pk_fp8_f32 v75, v12, v10 op_sel:[0,0,1]
	v_mul_f32_e32 v10, 0x41000000, v64
	v_mul_f32_e32 v6, 0x41000000, v6
	v_med3_f32 v10, v10, s25, v99
	v_med3_f32 v6, v6, s25, v99
	v_mov_b32_e32 v76, v51
	v_pk_mul_f32 v[82:83], v[62:63], v[112:113]
	v_pk_mul_f32 v[80:81], v[8:9], v[80:81]
	v_cvt_pk_fp8_f32 v76, v10, v6
	v_mul_f32_e32 v62, v82, v83
	v_mul_f32_e32 v8, v80, v81
	v_mul_f32_e32 v12, 0x41000000, v62
	v_mul_f32_e32 v6, 0x41000000, v8
	v_med3_f32 v8, v12, s25, v99
	v_med3_f32 v6, v6, s25, v99
	v_cvt_pk_fp8_f32 v76, v8, v6 op_sel:[0,0,1]
	v_mul_f32_e32 v6, 0x41000000, v60
	v_mul_f32_e32 v8, 0x41000000, v77
	v_med3_f32 v6, v6, s25, v99
	v_med3_f32 v8, v8, s25, v99
	v_mov_b32_e32 v77, v51
	v_cvt_pk_fp8_f32 v77, v6, v8
	v_mul_f32_e32 v2, 0x41000000, v2
	v_mul_f32_e32 v4, 0x41000000, v4
	v_med3_f32 v2, v2, s25, v99
	v_med3_f32 v4, v4, s25, v99
	v_cvt_pk_fp8_f32 v77, v2, v4 op_sel:[0,0,1]
	v_lshl_add_u64 v[78:79], v[56:57], 0, s[16:17]
	global_store_dwordx4 v[78:79], v[74:77], off
	s_cbranch_scc1 .LBB0_924
; __device__ __forceinline__ void phase4_post(const Args& a, LAS unsigned char* lds, int lane, int wave, int vcu, int G) {
;     ...
;         for (int h2 = 0; h2 < 2; ++h2) { const int t = t0 + h2 * G * 8; if (t < NT) {
;         const size_t o = (size_t)t * 1024 + 16 * lane;
;         const v4u f0 = __builtin_nontemporal_load((const v4u*)(OF + o)), f1 = __builtin_nontemporal_load((const v4u*)(OF + o + 8)), b0 = __builtin_nontemporal_load((const v4u*)(OB + o)), b1 = __builtin_nontemporal_load((const v4u*)(OB + o + 8)), r0 = __builtin_nontemporal_load((const v4u*)(Rr + o)), r1 = __builtin_nontemporal_load((const v4u*)(Rr + o + 8));
;         float x[16], r[16];
; #pragma unroll
;         for (int w = 0; w < 4; ++w) { x[2 * w] = bflo(f0[w]) + bflo(b0[w]); x[2 * w + 1] = bfhi(f0[w]) + bfhi(b0[w]); x[8 + 2 * w] = bflo(f1[w]) + bflo(b1[w]); x[8 + 2 * w + 1] = bfhi(f1[w]) + bfhi(b1[w]);
;             r[2 * w] = bflo(r0[w]); r[2 * w + 1] = bfhi(r0[w]); r[8 + 2 * w] = bflo(r1[w]); r[8 + 2 * w + 1] = bfhi(r1[w]); }
;         float ss = 0.f;
; #pragma unroll
;         for (int q = 0; q < 16; ++q) ss += x[q] * x[q];
;         ss += dppf<0xB1>(ss); ss += dppf<0x4E>(ss); ss += dppf<0x141>(ss); ss += dppf<0x140>(ss);
;         const float sc = rsqrtf(ss * (1.f / 256.f) + EPS);
	s_ashr_i32 s15, s14, 31
	s_lshl_b64 s[16:17], s[14:15], 11
	s_waitcnt vmcnt(12)
	v_lshlrev_b32_e32 v4, 16, v132
	v_lshlrev_b32_e32 v2, 16, v128
	v_and_b32_e32 v6, 0xffff0000, v132
	v_and_b32_e32 v8, 0xffff0000, v128
	s_waitcnt vmcnt(11)
	v_lshlrev_b32_e32 v10, 16, v136
	s_waitcnt vmcnt(10)
	v_lshlrev_b32_e32 v12, 16, v140
	v_lshlrev_b32_e32 v58, 16, v129
	v_lshlrev_b32_e32 v60, 16, v133
	v_lshlrev_b32_e32 v66, 16, v130
	v_lshlrev_b32_e32 v68, 16, v134
	v_add_f32_e32 v2, v4, v2
	v_add_f32_e32 v4, v6, v8
	v_add_f32_e32 v6, v12, v10
	v_add_f32_e32 v10, v60, v58
	v_add_f32_e32 v58, v68, v66
	v_mul_f32_e32 v68, v2, v2
	v_and_b32_e32 v62, 0xffff0000, v133
	v_and_b32_e32 v64, 0xffff0000, v129
	v_fmac_f32_e32 v68, v4, v4
	v_add_f32_e32 v12, v62, v64
	v_fmac_f32_e32 v68, v10, v10
	v_and_b32_e32 v70, 0xffff0000, v134
	v_and_b32_e32 v72, 0xffff0000, v130
	v_fmac_f32_e32 v68, v12, v12
	v_lshlrev_b32_e32 v129, 16, v131
	v_lshlrev_b32_e32 v133, 16, v135
	v_add_f32_e32 v60, v70, v72
	v_fmac_f32_e32 v68, v58, v58
	v_and_b32_e32 v135, 0xffff0000, v135
	v_and_b32_e32 v131, 0xffff0000, v131
	v_add_f32_e32 v62, v133, v129
	v_fmac_f32_e32 v68, v60, v60
	v_add_f32_e32 v64, v135, v131
	v_fmac_f32_e32 v68, v62, v62
	v_and_b32_e32 v14, 0xffff0000, v140
	v_and_b32_e32 v16, 0xffff0000, v136
	v_lshlrev_b32_e32 v111, 16, v141
	v_lshlrev_b32_e32 v113, 16, v137
	v_and_b32_e32 v110, 0xffff0000, v141
	v_and_b32_e32 v112, 0xffff0000, v137
	v_fmac_f32_e32 v68, v64, v64
	v_add_f32_e32 v8, v14, v16
	v_pk_add_f32 v[110:111], v[112:113], v[110:111]
	v_fmac_f32_e32 v68, v6, v6
	v_lshlrev_b32_e32 v117, 16, v142
	v_lshlrev_b32_e32 v119, 16, v138
	v_and_b32_e32 v116, 0xffff0000, v142
	v_and_b32_e32 v118, 0xffff0000, v138
	v_pk_mul_f32 v[112:113], v[110:111], v[110:111]
	v_fmac_f32_e32 v68, v8, v8
	v_lshlrev_b32_e32 v123, 16, v143
	v_and_b32_e32 v122, 0xffff0000, v143
	v_pk_add_f32 v[142:143], v[118:119], v[116:117]
	v_add_f32_e32 v68, v113, v68
	v_lshlrev_b32_e32 v125, 16, v139
	v_and_b32_e32 v124, 0xffff0000, v139
	v_pk_mul_f32 v[116:117], v[142:143], v[142:143]
	v_add_f32_e32 v68, v112, v68
	v_pk_add_f32 v[138:139], v[124:125], v[122:123]
	v_add_f32_e32 v68, v117, v68
	v_pk_mul_f32 v[118:119], v[138:139], v[138:139]
	v_add_f32_e32 v68, v116, v68
	v_add_f32_e32 v68, v119, v68
	v_add_f32_e32 v68, v118, v68
	s_waitcnt vmcnt(9)
	v_lshlrev_b32_e32 v108, 16, v144
	v_and_b32_e32 v144, 0xffff0000, v144
	v_add_f32_dpp v68, v68, v68 quad_perm:[1,0,3,2] row_mask:0xf bank_mask:0xf bound_ctrl:1
	v_mul_f32_e32 v14, 0xbfb8aa3b, v108
	v_mul_f32_e32 v16, 0xbfb8aa3b, v144
	v_add_f32_dpp v68, v68, v68 quad_perm:[2,3,0,1] row_mask:0xf bank_mask:0xf bound_ctrl:1
	v_exp_f32_e32 v14, v14
	v_exp_f32_e32 v16, v16
	v_add_f32_dpp v68, v68, v68 row_half_mirror row_mask:0xf bank_mask:0xf bound_ctrl:1
	s_waitcnt vmcnt(8)
; __device__ __forceinline__ float silu_f(float x) { return x * __builtin_amdgcn_rcpf(1.f + __expf(-x)); }
; __device__ __forceinline__ void phase4_post(const Args& a, LAS unsigned char* lds, int lane, int wave, int vcu, int G) {
;     ...
;         const float sc = rsqrtf(ss * (1.f / 256.f) + EPS);
;         float y[16];
; #pragma unroll
;         for (int q = 0; q < 16; ++q) y[q] = x[q] * sc * g4[q >> 2][q & 3] * silu_f(r[q]);
;         v4u o0;
; #pragma unroll
;         for (int w = 0; w < 4; ++w) o0[w] = pk4_fp8(y[4 * w] * SC_Y, y[4 * w + 1] * SC_Y, y[4 * w + 2] * SC_Y, y[4 * w + 3] * SC_Y);
;         *(v4u*)(Y + (size_t)t * 2048 + 16 * lane) = o0;
;         } }
	v_lshlrev_b32_e32 v140, 16, v148
	v_add_f32_e32 v14, 1.0, v14
	v_add_f32_dpp v68, v68, v68 row_mirror row_mask:0xf bank_mask:0xf bound_ctrl:1
	v_fmamk_f32 v68, v68, 0x3b800000, v94
	v_mul_f32_e32 v70, 0x4b800000, v68
	v_cmp_gt_f32_e32 vcc, s24, v68
	v_add_f32_e32 v16, 1.0, v16
	v_and_b32_e32 v88, 0xffff0000, v148
	v_cndmask_b32_e32 v68, v68, v70, vcc
	v_rsq_f32_e32 v68, v68
	v_lshlrev_b32_e32 v148, 16, v145
	v_rcp_f32_e32 v72, v14
	v_rcp_f32_e32 v14, v16
	v_mul_f32_e32 v16, 0x45800000, v68
	v_and_b32_e32 v114, 0xffff0000, v145
	v_mul_f32_e32 v66, 0xbfb8aa3b, v148
	v_cndmask_b32_e32 v129, v68, v16, vcc
	v_mul_f32_e32 v109, v2, v129
	v_mul_f32_e32 v145, v4, v129
	v_exp_f32_e32 v2, v66
	v_mul_f32_e32 v4, 0xbfb8aa3b, v114
	v_exp_f32_e32 v4, v4
	v_lshlrev_b32_e32 v120, 16, v146
	v_add_f32_e32 v2, 1.0, v2
	v_rcp_f32_e32 v70, v2
	v_add_f32_e32 v2, 1.0, v4
	v_and_b32_e32 v146, 0xffff0000, v146
	v_rcp_f32_e32 v16, v2
	v_mul_f32_e32 v2, 0xbfb8aa3b, v120
	v_exp_f32_e32 v2, v2
	v_mul_f32_e32 v4, 0xbfb8aa3b, v146
	v_exp_f32_e32 v4, v4
	v_lshlrev_b32_e32 v134, 16, v150
	v_add_f32_e32 v2, 1.0, v2
	v_and_b32_e32 v132, 0xffff0000, v150
	v_lshlrev_b32_e32 v150, 16, v147
	v_rcp_f32_e32 v68, v2
	v_add_f32_e32 v2, 1.0, v4
	v_lshlrev_b32_e32 v86, 16, v149
	v_and_b32_e32 v136, 0xffff0000, v149
	v_and_b32_e32 v126, 0xffff0000, v147
	v_mul_f32_e32 v149, v10, v129
	v_rcp_f32_e32 v10, v2
	v_mul_f32_e32 v2, 0xbfb8aa3b, v150
	v_exp_f32_e32 v2, v2
	v_mul_f32_e32 v4, 0xbfb8aa3b, v126
	v_exp_f32_e32 v4, v4
	v_mul_f32_e32 v115, v12, v129
	v_add_f32_e32 v2, 1.0, v2
	v_rcp_f32_e32 v66, v2
	v_add_f32_e32 v2, 1.0, v4
	v_rcp_f32_e32 v12, v2
	v_mul_f32_e32 v2, 0xbfb8aa3b, v140
	v_exp_f32_e32 v2, v2
	v_mul_f32_e32 v4, 0xbfb8aa3b, v88
	v_exp_f32_e32 v4, v4
	v_mul_f32_e32 v127, v64, v129
	v_add_f32_e32 v2, 1.0, v2
	v_rcp_f32_e32 v64, v2
	v_add_f32_e32 v2, 1.0, v4
	v_mul_f32_e32 v141, v6, v129
	v_rcp_f32_e32 v6, v2
	v_mul_f32_e32 v2, 0xbfb8aa3b, v86
	v_exp_f32_e32 v2, v2
	v_mul_f32_e32 v4, 0xbfb8aa3b, v136
	v_exp_f32_e32 v4, v4
	v_lshlrev_b32_e32 v130, 16, v151
	v_add_f32_e32 v2, 1.0, v2
	v_and_b32_e32 v128, 0xffff0000, v151
	v_mul_f32_e32 v151, v62, v129
	v_rcp_f32_e32 v62, v2
	v_add_f32_e32 v2, 1.0, v4
	v_mul_f32_e32 v89, v8, v129
	v_rcp_f32_e32 v8, v2
	v_mul_f32_e32 v2, 0xbfb8aa3b, v134
	v_exp_f32_e32 v2, v2
	v_mul_f32_e32 v4, 0xbfb8aa3b, v132
	v_exp_f32_e32 v4, v4
	v_mul_f32_e32 v147, v60, v129
	v_add_f32_e32 v2, 1.0, v2
	v_rcp_f32_e32 v60, v2
	v_add_f32_e32 v2, 1.0, v4
	v_rcp_f32_e32 v2, v2
	v_mul_f32_e32 v133, v142, v129
	v_mul_f32_e32 v4, 0xbfb8aa3b, v128
	v_exp_f32_e32 v4, v4
	v_pk_mul_f32 v[132:133], v[2:3], v[132:133]
	v_mul_f32_e32 v2, 0xbfb8aa3b, v130
	v_exp_f32_e32 v2, v2
	v_mul_f32_e32 v121, v58, v129
	v_pk_mul_f32 v[108:109], v[72:73], v[108:109]
	v_pk_mul_f32 v[144:145], v[14:15], v[144:145]
	v_add_f32_e32 v2, 1.0, v2
	v_rcp_f32_e32 v58, v2
	v_add_f32_e32 v2, 1.0, v4
	v_rcp_f32_e32 v4, v2
	v_mul_f32_e32 v14, v108, v109
	v_mul_f32_e32 v72, v144, v145
	v_mul_f32_e32 v87, v111, v129
	v_mul_f32_e32 v137, v110, v129
	v_mul_f32_e32 v135, v143, v129
	v_mul_f32_e32 v131, v139, v129
	v_mul_f32_e32 v129, v138, v129
	v_pk_mul_f32 v[130:131], v[58:59], v[130:131]
	v_pk_mul_f32 v[128:129], v[4:5], v[128:129]
	v_mul_f32_e32 v14, 0x41000000, v14
	v_mul_f32_e32 v58, 0x41000000, v72
	v_pk_mul_f32 v[144:145], v[70:71], v[148:149]
	v_mul_f32_e32 v4, v128, v129
	v_med3_f32 v14, v14, s25, v99
	v_med3_f32 v58, v58, s25, v99
	v_mov_b32_e32 v128, v51
	v_mul_f32_e32 v70, v144, v145
	v_pk_mul_f32 v[144:145], v[16:17], v[114:115]
	v_cvt_pk_fp8_f32 v128, v14, v58
	v_mul_f32_e32 v16, v144, v145
	v_pk_mul_f32 v[144:145], v[68:69], v[120:121]
	v_mul_f32_e32 v70, 0x41000000, v70
	v_mul_f32_e32 v68, v144, v145
	v_pk_mul_f32 v[144:145], v[10:11], v[146:147]
	v_mul_f32_e32 v14, 0x41000000, v16
	v_mul_f32_e32 v10, v144, v145
	v_med3_f32 v16, v70, s25, v99
	v_med3_f32 v14, v14, s25, v99
	v_cvt_pk_fp8_f32 v128, v16, v14 op_sel:[0,0,1]
	v_mul_f32_e32 v14, 0x41000000, v68
	v_mul_f32_e32 v10, 0x41000000, v10
	v_pk_mul_f32 v[144:145], v[66:67], v[150:151]
	v_med3_f32 v14, v14, s25, v99
	v_med3_f32 v10, v10, s25, v99
	v_mov_b32_e32 v129, v51
	v_mul_f32_e32 v66, v144, v145
	v_pk_mul_f32 v[144:145], v[12:13], v[126:127]
	v_cvt_pk_fp8_f32 v129, v14, v10
	v_mul_f32_e32 v12, v144, v145
	v_pk_mul_f32 v[140:141], v[64:65], v[140:141]
	v_pk_mul_f32 v[88:89], v[6:7], v[88:89]
	v_mul_f32_e32 v16, 0x41000000, v66
	v_mul_f32_e32 v10, 0x41000000, v12
	v_mul_f32_e32 v64, v140, v141
	v_mul_f32_e32 v6, v88, v89
	v_med3_f32 v12, v16, s25, v99
	v_med3_f32 v10, v10, s25, v99
	v_cvt_pk_fp8_f32 v129, v12, v10 op_sel:[0,0,1]
	v_mul_f32_e32 v10, 0x41000000, v64
	v_mul_f32_e32 v6, 0x41000000, v6
	v_mul_f32_e32 v2, v130, v131
	v_med3_f32 v10, v10, s25, v99
	v_med3_f32 v6, v6, s25, v99
	v_mov_b32_e32 v130, v51
	v_pk_mul_f32 v[86:87], v[62:63], v[86:87]
	v_pk_mul_f32 v[136:137], v[8:9], v[136:137]
	v_cvt_pk_fp8_f32 v130, v10, v6
	v_mul_f32_e32 v62, v86, v87
	v_mul_f32_e32 v8, v136, v137
	v_pk_mul_f32 v[134:135], v[60:61], v[134:135]
	v_mul_f32_e32 v12, 0x41000000, v62
	v_mul_f32_e32 v6, 0x41000000, v8
	v_mul_f32_e32 v60, v134, v135
	v_mul_f32_e32 v132, v132, v133
	v_med3_f32 v8, v12, s25, v99
	v_med3_f32 v6, v6, s25, v99
	v_cvt_pk_fp8_f32 v130, v8, v6 op_sel:[0,0,1]
	v_mul_f32_e32 v6, 0x41000000, v60
	v_mul_f32_e32 v8, 0x41000000, v132
	v_med3_f32 v6, v6, s25, v99
	v_med3_f32 v8, v8, s25, v99
	v_mov_b32_e32 v131, v51
	v_cvt_pk_fp8_f32 v131, v6, v8
	v_mul_f32_e32 v2, 0x41000000, v2
	v_mul_f32_e32 v4, 0x41000000, v4
	v_med3_f32 v2, v2, s25, v99
	v_med3_f32 v4, v4, s25, v99
	v_cvt_pk_fp8_f32 v131, v2, v4 op_sel:[0,0,1]
	v_lshl_add_u64 v[132:133], v[56:57], 0, s[16:17]
	global_store_dwordx4 v[132:133], v[128:131], off
	s_branch .LBB0_924
